# v049 + LN1 four-row absmax wave reductions rewritten with DPP (no ds_bpermute)
# speedup vs baseline: 1.0014x; 1.0014x over previous
; __device__ __forceinline__ float bflo(unsigned w) { return __uint_as_float(w << 16); }
; __device__ __forceinline__ float bfhi(unsigned w) { return __uint_as_float(w & 0xffff0000u); }
; template <bool WB = true>
; __device__ __forceinline__ void ln1_phase(const bf16_t* buf, bf16_t* h1b, unsigned* xqs, float* sx, const float* gam, const float* bet, int G, int b) {
;     ...
;     for (int row0 = gw; row0 < S_; row0 += R * NGW) {
;         f32x4 v[R][8]; float sum[R], sq[R], amax[R];
; #pragma unroll
;         for (int q = 0; q < R; ++q) {
;             const int row = min(row0 + q * NGW, S_ - 1);
;             const bf16_t* rp = buf + (size_t)row * D_;
;             sum[q] = 0.f;
; #pragma unroll
;             for (int j = 0; j < 8; ++j) { const u32x2 w = *(const u32x2*)(rp + 256 * j + 4 * lane); v[q][j] = (f32x4){bflo(w.x), bfhi(w.x), bflo(w.y), bfhi(w.y)}; sum[q] += (v[q][j].x + v[q][j].y) + (v[q][j].z + v[q][j].w); }
;         }
.LBB0_543:
	v_mbcnt_lo_u32_b32 v219, -1, 0
	v_mbcnt_hi_u32_b32 v219, -1, v219
	s_add_u32 s30, s92, 0x17800000
	s_addc_u32 s31, s93, 0
	v_lshlrev_b32_e32 v219, 3, v219
	s_lshl_b32 s20, s4, 12
	s_add_u32 s20, s30, s20
	s_addc_u32 s21, s31, 0
	s_add_i32 s22, s62, s4
	s_min_i32 s22, s22, 0x3fff
	s_lshl_b32 s22, s22, 12
	s_add_u32 s22, s30, s22
	s_addc_u32 s23, s31, 0
	s_add_i32 s24, s5, s4
	s_min_i32 s24, s24, 0x3fff
	s_lshl_b32 s24, s24, 12
	s_add_u32 s24, s30, s24
	s_addc_u32 s25, s31, 0
	s_mul_i32 s26, s96, 24
	s_add_i32 s26, s26, s4
	s_min_i32 s26, s26, 0x3fff
	s_lshl_b32 s26, s26, 12
	s_add_u32 s26, s30, s26
	s_addc_u32 s27, s31, 0
	global_load_dwordx2 v[224:225], v219, s[20:21]
	global_load_dwordx2 v[226:227], v219, s[20:21] offset:512
	global_load_dwordx2 v[228:229], v219, s[20:21] offset:3584
	global_load_dwordx2 v[230:231], v219, s[20:21] offset:1536
	global_load_dwordx2 v[232:233], v219, s[20:21] offset:1024
	global_load_dwordx2 v[234:235], v219, s[20:21] offset:2048
	global_load_dwordx2 v[236:237], v219, s[20:21] offset:2560
	global_load_dwordx2 v[238:239], v219, s[20:21] offset:3072
	global_load_dwordx2 v[240:241], v219, s[22:23]
	global_load_dwordx2 v[244:245], v219, s[22:23] offset:512
	global_load_dwordx2 v[246:247], v219, s[22:23] offset:3584
	global_load_dwordx2 v[248:249], v219, s[22:23] offset:1536
	global_load_dwordx2 v[250:251], v219, s[22:23] offset:1024
	global_load_dwordx2 v[252:253], v219, s[22:23] offset:2048
	global_load_dwordx2 v[254:255], v219, s[22:23] offset:2560
	v_lshl_add_u64 v[44:45], s[92:93], 0, v[38:39]
	s_waitcnt vmcnt(14)
	v_mov_b64_e32 v[2:3], v[224:225]
	global_load_dwordx2 v[224:225], v219, s[22:23] offset:3072
	s_waitcnt vmcnt(14)
	v_mov_b64_e32 v[4:5], v[226:227]
	global_load_dwordx2 v[226:227], v219, s[24:25]
	s_add_i32 s56, s62, s4
	s_min_i32 s0, s56, 0x3fff
	s_ashr_i32 s1, s0, 31
	s_lshl_b64 s[0:1], s[0:1], 12
	s_add_i32 s58, s5, s4
	s_waitcnt vmcnt(14)
	v_mov_b64_e32 v[50:51], v[228:229]
	global_load_dwordx2 v[228:229], v219, s[24:25] offset:512
	v_lshlrev_b32_e32 v140, 16, v2
	v_lshlrev_b32_e32 v141, 16, v4
	v_and_b32_e32 v143, 0xffff0000, v4
	v_and_b32_e32 v142, 0xffff0000, v2
	v_lshlrev_b32_e32 v137, 16, v5
	v_lshlrev_b32_e32 v136, 16, v3
	v_and_b32_e32 v139, 0xffff0000, v5
	v_and_b32_e32 v138, 0xffff0000, v3
	v_pk_add_f32 v[2:3], v[140:141], v[142:143]
	v_pk_add_f32 v[4:5], v[136:137], v[138:139]
	v_lshlrev_b32_e32 v43, 16, v51
	v_pk_add_f32 v[2:3], v[2:3], v[4:5]
	s_waitcnt vmcnt(14)
	v_mov_b64_e32 v[4:5], v[230:231]
	global_load_dwordx2 v[230:231], v219, s[24:25] offset:3584
	v_add_f32_e32 v2, 0, v2
	v_add_f32_e32 v8, v2, v3
	s_waitcnt vmcnt(14)
	v_mov_b64_e32 v[2:3], v[232:233]
	global_load_dwordx2 v[232:233], v219, s[24:25] offset:1536
	v_and_b32_e32 v41, 0xffff0000, v51
	v_lshlrev_b32_e32 v64, 16, v4
	v_and_b32_e32 v65, 0xffff0000, v4
	v_lshlrev_b32_e32 v66, 16, v5
	v_and_b32_e32 v67, 0xffff0000, v5
	s_waitcnt vmcnt(14)
	v_mov_b64_e32 v[4:5], v[234:235]
	global_load_dwordx2 v[234:235], v219, s[24:25] offset:1024
	v_lshlrev_b32_e32 v77, 16, v3
	v_lshlrev_b32_e32 v76, 16, v2
	v_and_b32_e32 v145, 0xffff0000, v3
	v_and_b32_e32 v144, 0xffff0000, v2
	v_pk_add_f32 v[2:3], v[76:77], v[144:145]
	v_add_f32_e32 v58, v64, v65
	v_pk_add_f32 v[2:3], v[2:3], v[2:3] op_sel:[0,1] op_sel_hi:[1,0]
	v_add_f32_e32 v56, v66, v67
	v_and_b32_e32 v61, 0xffff0000, v4
	s_waitcnt lgkmcnt(0)
	v_lshlrev_b32_e32 v9, 16, v4
	v_lshlrev_b32_e32 v59, 16, v5
	v_and_b32_e32 v57, 0xffff0000, v5
	v_mov_b32_e32 v3, v61
	v_pk_add_f32 v[2:3], v[8:9], v[2:3]
	v_pk_add_f32 v[4:5], v[58:59], v[56:57]
	s_nop 0
	v_pk_add_f32 v[46:47], v[2:3], v[4:5]
	s_waitcnt vmcnt(14)
	v_mov_b64_e32 v[2:3], v[236:237]
	global_load_dwordx2 v[236:237], v219, s[24:25] offset:2048
	s_waitcnt vmcnt(14)
	v_mov_b64_e32 v[4:5], v[238:239]
	global_load_dwordx2 v[238:239], v219, s[24:25] offset:2560
	v_lshlrev_b32_e32 v44, 16, v50
	v_and_b32_e32 v45, 0xffff0000, v50
	v_pk_add_f32 v[46:47], v[46:47], v[46:47] op_sel:[0,1] op_sel_hi:[1,0]
	v_lshl_add_u64 v[50:51], v[12:13], 0, s[0:1]
	v_mov_b32_e32 v47, v44
	s_min_i32 s0, s58, 0x3fff
	s_ashr_i32 s1, s0, 31
	s_lshl_b64 s[0:1], s[0:1], 12
	v_lshlrev_b32_e32 v7, 16, v3
	v_lshlrev_b32_e32 v6, 16, v2
	v_and_b32_e32 v147, 0xffff0000, v3
	v_and_b32_e32 v146, 0xffff0000, v2
	v_pk_add_f32 v[48:49], v[6:7], v[146:147]
	v_lshlrev_b32_e32 v2, 16, v4
	v_and_b32_e32 v3, 0xffff0000, v4
	v_lshlrev_b32_e32 v4, 16, v5
	v_and_b32_e32 v5, 0xffff0000, v5
	v_pk_add_f32 v[48:49], v[48:49], v[48:49] op_sel:[0,1] op_sel_hi:[1,0]
	v_add_f32_e32 v42, v2, v3
	v_add_f32_e32 v40, v4, v5
	v_mov_b32_e32 v49, v45
	v_pk_add_f32 v[46:47], v[46:47], v[48:49]
	v_pk_add_f32 v[48:49], v[42:43], v[40:41]
	s_nop 0
	v_pk_add_f32 v[46:47], v[46:47], v[48:49]
	s_nop 0
	v_add_f32_e32 v8, v46, v47
	s_waitcnt vmcnt(14)
	v_mov_b64_e32 v[46:47], v[240:241]
	global_load_dwordx2 v[240:241], v219, s[24:25] offset:3072
	s_waitcnt vmcnt(14)
	v_mov_b64_e32 v[48:49], v[244:245]
	global_load_dwordx2 v[244:245], v219, s[26:27]
	s_waitcnt vmcnt(14)
	v_mov_b64_e32 v[82:83], v[246:247]
	global_load_dwordx2 v[246:247], v219, s[26:27] offset:512
	v_lshlrev_b32_e32 v156, 16, v46
	v_lshlrev_b32_e32 v157, 16, v48
	v_and_b32_e32 v159, 0xffff0000, v48
	v_and_b32_e32 v158, 0xffff0000, v46
	v_lshlrev_b32_e32 v153, 16, v49
	v_lshlrev_b32_e32 v152, 16, v47
	v_and_b32_e32 v155, 0xffff0000, v49
	v_and_b32_e32 v154, 0xffff0000, v47
	v_pk_add_f32 v[46:47], v[156:157], v[158:159]
	v_pk_add_f32 v[48:49], v[152:153], v[154:155]
	s_nop 0
	v_pk_add_f32 v[46:47], v[46:47], v[48:49]
	s_waitcnt vmcnt(14)
; __device__ __forceinline__ float bflo(unsigned w) { return __uint_as_float(w << 16); }
; __device__ __forceinline__ float bfhi(unsigned w) { return __uint_as_float(w & 0xffff0000u); }
; template <bool WB = true>
; __device__ __forceinline__ void ln1_phase(const bf16_t* buf, bf16_t* h1b, unsigned* xqs, float* sx, const float* gam, const float* bet, int G, int b) {
;     ...
;             for (int j = 0; j < 8; ++j) { const u32x2 w = *(const u32x2*)(rp + 256 * j + 4 * lane); v[q][j] = (f32x4){bflo(w.x), bfhi(w.x), bflo(w.y), bfhi(w.y)}; sum[q] += (v[q][j].x + v[q][j].y) + (v[q][j].z + v[q][j].w); }
;         }
; #pragma unroll
;         for (int q = 0; q < R; ++q) sum[q] = wave_sum(sum[q]) * (1.0f / D_);
; #pragma unroll
;         for (int q = 0; q < R; ++q) { sq[q] = 0.f;
; #pragma unroll
;             for (int j = 0; j < 8; ++j) { v[q][j] = v[q][j] - sum[q]; sq[q] += (v[q][j].x * v[q][j].x + v[q][j].y * v[q][j].y) + (v[q][j].z * v[q][j].z + v[q][j].w * v[q][j].w); } }
	v_mov_b64_e32 v[48:49], v[248:249]
	global_load_dwordx2 v[248:249], v219, s[26:27] offset:3584
	v_add_f32_e32 v10, 0, v46
	v_add_f32_e32 v68, v10, v47
	s_waitcnt vmcnt(14)
	v_mov_b64_e32 v[46:47], v[250:251]
	global_load_dwordx2 v[250:251], v219, s[26:27] offset:1536
	v_lshlrev_b32_e32 v84, 16, v48
	v_and_b32_e32 v85, 0xffff0000, v48
	v_lshlrev_b32_e32 v86, 16, v49
	v_and_b32_e32 v87, 0xffff0000, v49
	s_waitcnt vmcnt(14)
	v_mov_b64_e32 v[48:49], v[252:253]
	global_load_dwordx2 v[252:253], v219, s[26:27] offset:1024
	v_lshlrev_b32_e32 v89, 16, v47
	v_lshlrev_b32_e32 v88, 16, v46
	v_and_b32_e32 v151, 0xffff0000, v47
	v_and_b32_e32 v150, 0xffff0000, v46
	v_pk_add_f32 v[46:47], v[88:89], v[150:151]
	v_add_f32_e32 v72, v84, v85
	v_pk_add_f32 v[46:47], v[46:47], v[46:47] op_sel:[0,1] op_sel_hi:[1,0]
	v_add_f32_e32 v70, v86, v87
	v_and_b32_e32 v75, 0xffff0000, v48
	v_lshlrev_b32_e32 v69, 16, v48
	v_lshlrev_b32_e32 v73, 16, v49
	v_and_b32_e32 v71, 0xffff0000, v49
	v_mov_b32_e32 v47, v75
	v_pk_add_f32 v[46:47], v[68:69], v[46:47]
	v_pk_add_f32 v[48:49], v[72:73], v[70:71]
	s_nop 0
	v_pk_add_f32 v[78:79], v[46:47], v[48:49]
	s_waitcnt vmcnt(14)
	v_mov_b64_e32 v[46:47], v[254:255]
	global_load_dwordx2 v[254:255], v219, s[26:27] offset:2048
	v_pk_add_f32 v[78:79], v[78:79], v[78:79] op_sel:[0,1] op_sel_hi:[1,0]
	v_lshlrev_b32_e32 v49, 16, v83
	v_lshlrev_b32_e32 v63, 16, v47
	v_lshlrev_b32_e32 v62, 16, v46
	v_and_b32_e32 v149, 0xffff0000, v47
	v_and_b32_e32 v148, 0xffff0000, v46
	s_waitcnt vmcnt(14)
	v_mov_b64_e32 v[46:47], v[224:225]
	global_load_dwordx2 v[224:225], v219, s[26:27] offset:2560
	v_pk_add_f32 v[80:81], v[62:63], v[148:149]
	v_lshlrev_b32_e32 v50, 16, v82
	v_and_b32_e32 v51, 0xffff0000, v82
	v_pk_add_f32 v[80:81], v[80:81], v[80:81] op_sel:[0,1] op_sel_hi:[1,0]
	v_mov_b32_e32 v79, v50
	v_mov_b32_e32 v81, v51
	v_pk_add_f32 v[78:79], v[78:79], v[80:81]
	v_lshlrev_b32_e32 v52, 16, v46
	v_and_b32_e32 v53, 0xffff0000, v46
	v_lshlrev_b32_e32 v54, 16, v47
	v_and_b32_e32 v55, 0xffff0000, v47
	v_add_f32_e32 v48, v52, v53
	v_add_f32_e32 v46, v54, v55
	v_and_b32_e32 v47, 0xffff0000, v83
	v_pk_add_f32 v[80:81], v[48:49], v[46:47]
	v_lshl_add_u64 v[82:83], v[12:13], 0, s[0:1]
	v_pk_add_f32 v[78:79], v[78:79], v[80:81]
	s_mul_i32 s0, s96, 24
	v_add_f32_e32 v10, v78, v79
	s_waitcnt vmcnt(14)
	v_mov_b64_e32 v[78:79], v[226:227]
	global_load_dwordx2 v[226:227], v219, s[26:27] offset:3072
	s_waitcnt vmcnt(14)
	v_mov_b64_e32 v[80:81], v[228:229]
	s_add_i32 s60, s0, s4
	s_min_i32 s0, s60, 0x3fff
	s_ashr_i32 s1, s0, 31
	s_lshl_b64 s[0:1], s[0:1], 12
	s_nop 1
	s_waitcnt vmcnt(13)
	v_mov_b64_e32 v[100:101], v[230:231]
	s_waitcnt lgkmcnt(0)
	v_add_f32_dpp v8, v8, v8 quad_perm:[1,0,3,2] row_mask:0xf bank_mask:0xf
	s_nop 1
	s_waitcnt lgkmcnt(0)
	v_add_f32_dpp v8, v8, v8 quad_perm:[2,3,0,1] row_mask:0xf bank_mask:0xf
	s_nop 1
	s_waitcnt lgkmcnt(0)
	v_add_f32_dpp v8, v8, v8 row_half_mirror row_mask:0xf bank_mask:0xf
	s_nop 1
	s_waitcnt lgkmcnt(0)
	v_add_f32_dpp v8, v8, v8 row_mirror row_mask:0xf bank_mask:0xf
	s_nop 1
	s_waitcnt lgkmcnt(0)
	v_add_f32_dpp v8, v8, v8 row_bcast:15 row_mask:0xa bank_mask:0xf
	s_nop 1
	s_waitcnt lgkmcnt(0)
	v_add_f32_dpp v56, v8, v8 row_bcast:31 row_mask:0xc bank_mask:0xf
	s_nop 1
	v_readlane_b32 s98, v56, 63
	s_nop 1
	v_mov_b32_e32 v56, s98
	s_nop 1
	v_fmac_f32_e32 v142, 0xba000000, v56
	v_fmac_f32_e32 v143, 0xba000000, v56
	v_fmac_f32_e32 v138, 0xba000000, v56
	v_fmac_f32_e32 v140, 0xba000000, v56
	s_waitcnt lgkmcnt(0)
	v_add_f32_dpp v8, v10, v10 quad_perm:[1,0,3,2] row_mask:0xf bank_mask:0xf
	s_nop 1
	v_fmac_f32_e32 v139, 0xba000000, v56
	v_fmac_f32_e32 v141, 0xba000000, v56
	v_mov_b32_e32 v185, v142
	v_fmac_f32_e32 v136, 0xba000000, v56
	s_waitcnt lgkmcnt(0)
	v_add_f32_dpp v8, v8, v8 quad_perm:[2,3,0,1] row_mask:0xf bank_mask:0xf
	s_nop 1
	v_fmac_f32_e32 v137, 0xba000000, v56
	v_mov_b32_e32 v184, v140
	v_fmac_f32_e32 v144, 0xba000000, v56
	v_fmac_f32_e32 v145, 0xba000000, v56
	s_waitcnt lgkmcnt(0)
	v_add_f32_dpp v8, v8, v8 row_half_mirror row_mask:0xf bank_mask:0xf
	s_nop 1
	v_fmac_f32_e32 v77, 0xba000000, v56
	v_fmac_f32_e32 v76, 0xba000000, v56
	v_fmac_f32_e32 v64, 0xba000000, v56
	v_fmac_f32_e32 v65, 0xba000000, v56
	s_waitcnt lgkmcnt(0)
	v_add_f32_dpp v8, v8, v8 row_mirror row_mask:0xf bank_mask:0xf
	s_nop 1
	v_fmac_f32_e32 v66, 0xba000000, v56
	v_fmac_f32_e32 v67, 0xba000000, v56
	v_fmac_f32_e32 v57, 0xba000000, v56
	v_fmac_f32_e32 v59, 0xba000000, v56
	s_waitcnt lgkmcnt(0)
	v_add_f32_dpp v8, v8, v8 row_bcast:15 row_mask:0xa bank_mask:0xf
	s_nop 1
	v_fmac_f32_e32 v61, 0xba000000, v56
	v_fmac_f32_e32 v9, 0xba000000, v56
	v_fmac_f32_e32 v146, 0xba000000, v56
	v_fmac_f32_e32 v147, 0xba000000, v56
	s_waitcnt lgkmcnt(0)
	v_add_f32_dpp v48, v8, v8 row_bcast:31 row_mask:0xc bank_mask:0xf
	s_nop 1
	v_readlane_b32 s98, v48, 63
	s_nop 1
	v_mov_b32_e32 v48, s98
	v_fmac_f32_e32 v7, 0xba000000, v56
	v_fmac_f32_e32 v6, 0xba000000, v56
	v_lshlrev_b32_e32 v164, 16, v78
	v_lshlrev_b32_e32 v165, 16, v80
	v_and_b32_e32 v171, 0xffff0000, v80
	v_and_b32_e32 v170, 0xffff0000, v78
	v_lshlrev_b32_e32 v161, 16, v81
	v_lshlrev_b32_e32 v160, 16, v79
	v_and_b32_e32 v163, 0xffff0000, v81
	v_and_b32_e32 v162, 0xffff0000, v79
	v_pk_add_f32 v[78:79], v[164:165], v[170:171]
	v_pk_add_f32 v[80:81], v[160:161], v[162:163]
	v_fmac_f32_e32 v2, 0xba000000, v56
	v_pk_add_f32 v[78:79], v[78:79], v[80:81]
	s_waitcnt vmcnt(12)
	v_mov_b64_e32 v[80:81], v[232:233]
	v_add_f32_e32 v40, 0, v78
	v_add_f32_e32 v90, v40, v79
	s_waitcnt vmcnt(11)
; __device__ __forceinline__ float bflo(unsigned w) { return __uint_as_float(w << 16); }
; __device__ __forceinline__ float bfhi(unsigned w) { return __uint_as_float(w & 0xffff0000u); }
; template <bool WB = true>
; __device__ __forceinline__ void ln1_phase(const bf16_t* buf, bf16_t* h1b, unsigned* xqs, float* sx, const float* gam, const float* bet, int G, int b) {
;     ...
;             for (int j = 0; j < 8; ++j) { const u32x2 w = *(const u32x2*)(rp + 256 * j + 4 * lane); v[q][j] = (f32x4){bflo(w.x), bfhi(w.x), bflo(w.y), bfhi(w.y)}; sum[q] += (v[q][j].x + v[q][j].y) + (v[q][j].z + v[q][j].w); }
;         }
; #pragma unroll
;         for (int q = 0; q < R; ++q) sum[q] = wave_sum(sum[q]) * (1.0f / D_);
; #pragma unroll
;         for (int q = 0; q < R; ++q) { sq[q] = 0.f;
; #pragma unroll
;             for (int j = 0; j < 8; ++j) { v[q][j] = v[q][j] - sum[q]; sq[q] += (v[q][j].x * v[q][j].x + v[q][j].y * v[q][j].y) + (v[q][j].z * v[q][j].z + v[q][j].w * v[q][j].w); } }
	v_mov_b64_e32 v[78:79], v[234:235]
	v_fmac_f32_e32 v3, 0xba000000, v56
	v_fmac_f32_e32 v4, 0xba000000, v56
	v_fmac_f32_e32 v5, 0xba000000, v56
	v_fmac_f32_e32 v41, 0xba000000, v56
	v_fmac_f32_e32 v43, 0xba000000, v56
	v_fmac_f32_e32 v45, 0xba000000, v56
	v_fmac_f32_e32 v44, 0xba000000, v56
	v_fmac_f32_e32 v154, 0xba000000, v48
	v_fmac_f32_e32 v152, 0xba000000, v48
	v_fmac_f32_e32 v158, 0xba000000, v48
	v_fmac_f32_e32 v156, 0xba000000, v48
	v_fmac_f32_e32 v155, 0xba000000, v48
	v_fmac_f32_e32 v153, 0xba000000, v48
	v_fmac_f32_e32 v159, 0xba000000, v48
	v_fmac_f32_e32 v157, 0xba000000, v48
	v_fmac_f32_e32 v150, 0xba000000, v48
	v_fmac_f32_e32 v88, 0xba000000, v48
	v_fmac_f32_e32 v151, 0xba000000, v48
	v_fmac_f32_e32 v89, 0xba000000, v48
	v_fmac_f32_e32 v85, 0xba000000, v48
	v_fmac_f32_e32 v84, 0xba000000, v48
	v_fmac_f32_e32 v87, 0xba000000, v48
	v_fmac_f32_e32 v86, 0xba000000, v48
	v_fmac_f32_e32 v71, 0xba000000, v48
	v_fmac_f32_e32 v73, 0xba000000, v48
	v_fmac_f32_e32 v75, 0xba000000, v48
	v_fmac_f32_e32 v69, 0xba000000, v48
	v_fmac_f32_e32 v148, 0xba000000, v48
	v_fmac_f32_e32 v62, 0xba000000, v48
	v_fmac_f32_e32 v149, 0xba000000, v48
	v_fmac_f32_e32 v63, 0xba000000, v48
	v_fmac_f32_e32 v53, 0xba000000, v48
	v_fmac_f32_e32 v52, 0xba000000, v48
	v_fmac_f32_e32 v55, 0xba000000, v48
	v_fmac_f32_e32 v54, 0xba000000, v48
	v_fmac_f32_e32 v47, 0xba000000, v48
	v_fmac_f32_e32 v49, 0xba000000, v48
	v_fmac_f32_e32 v51, 0xba000000, v48
	v_fmac_f32_e32 v50, 0xba000000, v48
	v_mov_b32_e32 v186, v89
	v_mov_b32_e32 v187, v151
	v_mov_b32_e32 v89, v150
	v_pk_mul_f32 v[150:151], v[88:89], v[88:89]
	v_mov_b32_e32 v74, v69
	v_mov_b32_e32 v70, v73
	v_lshlrev_b32_e32 v112, 16, v80
	v_and_b32_e32 v113, 0xffff0000, v80
	v_lshlrev_b32_e32 v114, 16, v81
	v_and_b32_e32 v115, 0xffff0000, v81
	s_waitcnt vmcnt(10)
	v_mov_b64_e32 v[80:81], v[236:237]
	v_lshlrev_b32_e32 v105, 16, v79
	v_lshlrev_b32_e32 v104, 16, v78
	v_and_b32_e32 v173, 0xffff0000, v79
	v_and_b32_e32 v172, 0xffff0000, v78
	v_pk_add_f32 v[78:79], v[104:105], v[172:173]
	v_add_f32_e32 v108, v112, v113
	v_pk_add_f32 v[78:79], v[78:79], v[78:79] op_sel:[0,1] op_sel_hi:[1,0]
	v_add_f32_e32 v106, v114, v115
	v_and_b32_e32 v111, 0xffff0000, v80
	v_lshlrev_b32_e32 v91, 16, v80
	v_lshlrev_b32_e32 v109, 16, v81
	v_and_b32_e32 v107, 0xffff0000, v81
	v_mov_b32_e32 v79, v111
	v_pk_add_f32 v[78:79], v[90:91], v[78:79]
	v_pk_add_f32 v[80:81], v[108:109], v[106:107]
	s_nop 0
	v_pk_add_f32 v[96:97], v[78:79], v[80:81]
	s_waitcnt vmcnt(9)
	v_mov_b64_e32 v[78:79], v[238:239]
	v_pk_add_f32 v[96:97], v[96:97], v[96:97] op_sel:[0,1] op_sel_hi:[1,0]
	v_lshlrev_b32_e32 v81, 16, v101
	v_lshlrev_b32_e32 v103, 16, v79
	v_lshlrev_b32_e32 v102, 16, v78
	v_and_b32_e32 v175, 0xffff0000, v79
	v_and_b32_e32 v174, 0xffff0000, v78
	s_waitcnt vmcnt(8)
	v_mov_b64_e32 v[78:79], v[240:241]
	v_pk_add_f32 v[98:99], v[102:103], v[174:175]
	v_lshlrev_b32_e32 v82, 16, v100
	v_and_b32_e32 v83, 0xffff0000, v100
	v_pk_add_f32 v[98:99], v[98:99], v[98:99] op_sel:[0,1] op_sel_hi:[1,0]
	v_mov_b32_e32 v97, v82
	v_mov_b32_e32 v99, v83
	v_pk_add_f32 v[96:97], v[96:97], v[98:99]
	v_lshlrev_b32_e32 v92, 16, v78
	v_and_b32_e32 v93, 0xffff0000, v78
	v_lshlrev_b32_e32 v94, 16, v79
	v_and_b32_e32 v95, 0xffff0000, v79
	v_add_f32_e32 v80, v92, v93
	v_add_f32_e32 v78, v94, v95
	v_and_b32_e32 v79, 0xffff0000, v101
	v_pk_add_f32 v[98:99], v[80:81], v[78:79]
	v_lshl_add_u64 v[100:101], v[12:13], 0, s[0:1]
	v_pk_add_f32 v[96:97], v[96:97], v[98:99]
	s_nop 0
	v_add_f32_e32 v40, v96, v97
	s_waitcnt vmcnt(7)
	v_mov_b64_e32 v[96:97], v[244:245]
	s_waitcnt vmcnt(6)
	v_mov_b64_e32 v[98:99], v[246:247]
	s_waitcnt vmcnt(5)
	v_mov_b64_e32 v[182:183], v[248:249]
	s_nop 1
	s_waitcnt lgkmcnt(0)
	v_add_f32_dpp v8, v40, v40 quad_perm:[1,0,3,2] row_mask:0xf bank_mask:0xf
	s_nop 1
	s_waitcnt lgkmcnt(0)
	v_add_f32_dpp v8, v8, v8 quad_perm:[2,3,0,1] row_mask:0xf bank_mask:0xf
	s_nop 1
	s_waitcnt lgkmcnt(0)
	v_add_f32_dpp v8, v8, v8 row_half_mirror row_mask:0xf bank_mask:0xf
	s_nop 1
	s_waitcnt lgkmcnt(0)
	v_add_f32_dpp v8, v8, v8 row_mirror row_mask:0xf bank_mask:0xf
	s_nop 1
	s_waitcnt lgkmcnt(0)
	v_add_f32_dpp v8, v8, v8 row_bcast:15 row_mask:0xa bank_mask:0xf
	s_nop 1
	s_waitcnt lgkmcnt(0)
	v_add_f32_dpp v8, v8, v8 row_bcast:31 row_mask:0xc bank_mask:0xf
	s_nop 1
	v_readlane_b32 s98, v8, 63
	s_nop 1
	v_mov_b32_e32 v8, s98
	v_fmac_f32_e32 v162, 0xba000000, v8
	v_fmac_f32_e32 v170, 0xba000000, v8
	v_fmac_f32_e32 v163, 0xba000000, v8
	v_fmac_f32_e32 v171, 0xba000000, v8
	v_fmac_f32_e32 v160, 0xba000000, v8
	v_fmac_f32_e32 v164, 0xba000000, v8
	v_fmac_f32_e32 v161, 0xba000000, v8
	v_fmac_f32_e32 v165, 0xba000000, v8
	v_fmac_f32_e32 v172, 0xba000000, v8
	v_fmac_f32_e32 v173, 0xba000000, v8
	v_fmac_f32_e32 v105, 0xba000000, v8
	v_fmac_f32_e32 v104, 0xba000000, v8
	v_fmac_f32_e32 v112, 0xba000000, v8
	v_fmac_f32_e32 v113, 0xba000000, v8
	v_fmac_f32_e32 v114, 0xba000000, v8
	v_fmac_f32_e32 v115, 0xba000000, v8
	v_fmac_f32_e32 v107, 0xba000000, v8
	v_fmac_f32_e32 v109, 0xba000000, v8
	v_fmac_f32_e32 v111, 0xba000000, v8
	v_fmac_f32_e32 v91, 0xba000000, v8
	v_fmac_f32_e32 v174, 0xba000000, v8
	v_fmac_f32_e32 v175, 0xba000000, v8
	v_fmac_f32_e32 v103, 0xba000000, v8
	v_fmac_f32_e32 v102, 0xba000000, v8
	v_fmac_f32_e32 v92, 0xba000000, v8
	v_fmac_f32_e32 v93, 0xba000000, v8
	v_fmac_f32_e32 v94, 0xba000000, v8
	v_fmac_f32_e32 v95, 0xba000000, v8
	v_fmac_f32_e32 v79, 0xba000000, v8
	v_fmac_f32_e32 v81, 0xba000000, v8
	v_fmac_f32_e32 v83, 0xba000000, v8
	v_fmac_f32_e32 v82, 0xba000000, v8
	v_mov_b32_e32 v110, v91
	v_mov_b32_e32 v106, v109
	v_mov_b32_e32 v78, v81
	v_lshlrev_b32_e32 v190, 16, v96
	v_lshlrev_b32_e32 v191, 16, v98
	v_and_b32_e32 v193, 0xffff0000, v98
	v_and_b32_e32 v192, 0xffff0000, v96
	v_lshlrev_b32_e32 v179, 16, v99
	v_lshlrev_b32_e32 v178, 16, v97
	v_and_b32_e32 v189, 0xffff0000, v99
	v_and_b32_e32 v188, 0xffff0000, v97
	v_pk_add_f32 v[96:97], v[190:191], v[192:193]
	v_pk_add_f32 v[98:99], v[178:179], v[188:189]
	s_nop 0
	v_pk_add_f32 v[96:97], v[96:97], v[98:99]
	s_waitcnt vmcnt(4)
; template <bool WB = true>
; __device__ __forceinline__ void ln1_phase(const bf16_t* buf, bf16_t* h1b, unsigned* xqs, float* sx, const float* gam, const float* bet, int G, int b) {
;     ...
;         for (int q = 0; q < R; ++q) sum[q] = wave_sum(sum[q]) * (1.0f / D_);
; #pragma unroll
;         for (int q = 0; q < R; ++q) { sq[q] = 0.f;
; #pragma unroll
;             for (int j = 0; j < 8; ++j) { v[q][j] = v[q][j] - sum[q]; sq[q] += (v[q][j].x * v[q][j].x + v[q][j].y * v[q][j].y) + (v[q][j].z * v[q][j].z + v[q][j].w * v[q][j].w); } }
; #pragma unroll
;         for (int q = 0; q < R; ++q) sq[q] = 1.0f / sqrtf(wave_sum(sq[q]) * (1.0f / D_) + LN_EPS);
; #pragma unroll
;         for (int j = 0; j < 8; ++j) {
;             const f32x4 gg = *(const f32x4*)(gam + 256 * j + 4 * lane), bb = *(const f32x4*)(bet + 256 * j + 4 * lane);
	v_mov_b64_e32 v[98:99], v[250:251]
	v_add_f32_e32 v42, 0, v96
	v_add_f32_e32 v120, v42, v97
	s_waitcnt vmcnt(3)
	v_mov_b64_e32 v[96:97], v[252:253]
	v_lshlrev_b32_e32 v130, 16, v98
	v_and_b32_e32 v131, 0xffff0000, v98
	v_lshlrev_b32_e32 v132, 16, v99
	v_and_b32_e32 v133, 0xffff0000, v99
	s_waitcnt vmcnt(2)
	v_mov_b64_e32 v[98:99], v[254:255]
	v_lshlrev_b32_e32 v135, 16, v97
	v_lshlrev_b32_e32 v134, 16, v96
	v_and_b32_e32 v195, 0xffff0000, v97
	v_and_b32_e32 v194, 0xffff0000, v96
	v_pk_add_f32 v[96:97], v[134:135], v[194:195]
	v_add_f32_e32 v126, v130, v131
	v_pk_add_f32 v[96:97], v[96:97], v[96:97] op_sel:[0,1] op_sel_hi:[1,0]
	v_add_f32_e32 v124, v132, v133
	v_and_b32_e32 v129, 0xffff0000, v98
	v_lshlrev_b32_e32 v121, 16, v98
	v_lshlrev_b32_e32 v127, 16, v99
	v_and_b32_e32 v125, 0xffff0000, v99
	v_mov_b32_e32 v97, v129
	v_pk_add_f32 v[96:97], v[120:121], v[96:97]
	v_pk_add_f32 v[98:99], v[126:127], v[124:125]
	s_nop 0
	v_pk_add_f32 v[176:177], v[96:97], v[98:99]
	s_waitcnt vmcnt(1)
	v_mov_b64_e32 v[96:97], v[224:225]
	v_pk_add_f32 v[176:177], v[176:177], v[176:177] op_sel:[0,1] op_sel_hi:[1,0]
	v_lshlrev_b32_e32 v99, 16, v183
	v_lshlrev_b32_e32 v123, 16, v97
	v_lshlrev_b32_e32 v122, 16, v96
	v_and_b32_e32 v197, 0xffff0000, v97
	v_and_b32_e32 v196, 0xffff0000, v96
	s_waitcnt vmcnt(0)
	v_mov_b64_e32 v[96:97], v[226:227]
	global_load_dwordx4 v[224:227], v[14:15], off
	global_load_dwordx4 v[228:231], v[16:17], off
	global_load_dwordx4 v[232:235], v[14:15], off offset:1024
	global_load_dwordx4 v[236:239], v[16:17], off offset:1024
	global_load_dwordx4 v[244:247], v[14:15], off offset:2048
	global_load_dwordx4 v[248:251], v[16:17], off offset:2048
	global_load_dwordx4 v[252:255], v[14:15], off offset:3072
	v_pk_add_f32 v[180:181], v[122:123], v[196:197]
	v_lshlrev_b32_e32 v100, 16, v182
	v_and_b32_e32 v101, 0xffff0000, v182
	v_pk_add_f32 v[180:181], v[180:181], v[180:181] op_sel:[0,1] op_sel_hi:[1,0]
	v_mov_b32_e32 v177, v100
	v_mov_b32_e32 v181, v101
	v_pk_add_f32 v[176:177], v[176:177], v[180:181]
	v_mov_b32_e32 v182, v137
	v_lshlrev_b32_e32 v116, 16, v96
	v_and_b32_e32 v117, 0xffff0000, v96
	v_lshlrev_b32_e32 v118, 16, v97
	v_and_b32_e32 v119, 0xffff0000, v97
	v_add_f32_e32 v98, v116, v117
	v_add_f32_e32 v96, v118, v119
	v_and_b32_e32 v97, 0xffff0000, v183
	v_pk_add_f32 v[180:181], v[98:99], v[96:97]
	v_mov_b32_e32 v183, v139
	v_pk_add_f32 v[176:177], v[176:177], v[180:181]
	v_mov_b32_e32 v181, v143
	v_add_f32_e32 v42, v176, v177
	s_nop 1
	v_pk_mul_f32 v[142:143], v[142:143], v[142:143]
	v_mov_b32_e32 v180, v141
	v_pk_fma_f32 v[140:141], v[140:141], v[140:141], v[142:143]
	v_mov_b32_e32 v143, v138
	s_waitcnt lgkmcnt(0)
	v_add_f32_dpp v10, v42, v42 quad_perm:[1,0,3,2] row_mask:0xf bank_mask:0xf
	s_nop 1
	v_pk_mul_f32 v[138:139], v[138:139], v[138:139]
	v_mov_b32_e32 v142, v136
	v_pk_fma_f32 v[136:137], v[136:137], v[136:137], v[138:139]
	v_mov_b32_e32 v176, v77
	s_waitcnt lgkmcnt(0)
	v_add_f32_dpp v10, v10, v10 quad_perm:[2,3,0,1] row_mask:0xf bank_mask:0xf
	s_nop 1
	v_mov_b32_e32 v177, v145
	v_mov_b32_e32 v77, v144
	v_pk_add_f32 v[136:137], v[140:141], v[136:137]
	v_pk_mul_f32 v[138:139], v[176:177], v[176:177]
	s_waitcnt lgkmcnt(0)
	v_add_f32_dpp v10, v10, v10 row_half_mirror row_mask:0xf bank_mask:0xf
	s_nop 1
	v_pk_mul_f32 v[140:141], v[76:77], v[76:77]
	v_pk_add_f32 v[136:137], v[136:137], v[136:137] op_sel_hi:[0,1]
	v_pk_mov_b32 v[144:145], v[140:141], v[138:139] op_sel:[1,0]
	v_mov_b32_e32 v141, v139
	s_waitcnt lgkmcnt(0)
	v_add_f32_dpp v10, v10, v10 row_mirror row_mask:0xf bank_mask:0xf
	s_nop 1
	v_pk_add_f32 v[138:139], v[144:145], v[140:141]
	v_mul_f32_e32 v136, v57, v57
	v_pk_add_f32 v[138:139], v[138:139], v[138:139] op_sel_hi:[0,1]
	v_mul_f32_e32 v138, v59, v59
	s_waitcnt lgkmcnt(0)
	v_add_f32_dpp v10, v10, v10 row_bcast:15 row_mask:0xa bank_mask:0xf
	s_nop 1
	v_pk_add_f32 v[136:137], v[138:139], v[136:137]
	s_waitcnt lgkmcnt(0)
	v_add_f32_dpp v46, v10, v10 row_bcast:31 row_mask:0xc bank_mask:0xf
	s_nop 1
	v_readlane_b32 s98, v46, 63
	s_nop 1
	v_mov_b32_e32 v46, s98
	v_mul_f32_e32 v10, v64, v64
	v_pk_fma_f32 v[140:141], v[64:65], v[64:65], v[10:11] op_sel_hi:[1,1,0]
	v_mul_f32_e32 v10, v66, v66
	v_pk_fma_f32 v[144:145], v[66:67], v[66:67], v[10:11] op_sel_hi:[1,1,0]
	v_mul_f32_e32 v140, v9, v9
	v_mul_f32_e32 v144, v61, v61
	v_pk_add_f32 v[140:141], v[140:141], v[144:145]
	v_mul_f32_e32 v10, v2, v2
	v_pk_add_f32 v[136:137], v[140:141], v[136:137]
	v_mov_b32_e32 v140, v7
	v_mov_b32_e32 v141, v147
	v_mov_b32_e32 v7, v146
	v_pk_mul_f32 v[138:139], v[140:141], v[140:141]
	v_pk_mul_f32 v[144:145], v[6:7], v[6:7]
	v_pk_add_f32 v[136:137], v[136:137], v[136:137] op_sel_hi:[0,1]
	v_pk_mov_b32 v[146:147], v[144:145], v[138:139] op_sel:[1,0]
	v_mov_b32_e32 v145, v139
	v_pk_add_f32 v[138:139], v[146:147], v[144:145]
	v_pk_fma_f32 v[144:145], v[2:3], v[2:3], v[10:11] op_sel_hi:[1,1,0]
	v_mul_f32_e32 v10, v4, v4
	v_pk_add_f32 v[138:139], v[138:139], v[138:139] op_sel_hi:[0,1]
	v_pk_fma_f32 v[146:147], v[4:5], v[4:5], v[10:11] op_sel_hi:[1,1,0]
	v_mul_f32_e32 v144, v44, v44
	v_mul_f32_e32 v146, v45, v45
	v_mul_f32_e32 v138, v43, v43
	v_mul_f32_e32 v136, v41, v41
	v_pk_add_f32 v[144:145], v[144:145], v[146:147]
	v_pk_add_f32 v[136:137], v[138:139], v[136:137]
	v_fmac_f32_e32 v188, 0xba000000, v46
	v_pk_add_f32 v[136:137], v[144:145], v[136:137]
	v_fmac_f32_e32 v178, 0xba000000, v46
	v_add_f32_e32 v10, v136, v137
	v_fmac_f32_e32 v192, 0xba000000, v46
	v_fmac_f32_e32 v190, 0xba000000, v46
	v_fmac_f32_e32 v189, 0xba000000, v46
	v_fmac_f32_e32 v179, 0xba000000, v46
	v_fmac_f32_e32 v193, 0xba000000, v46
	v_fmac_f32_e32 v191, 0xba000000, v46
	v_fmac_f32_e32 v194, 0xba000000, v46
	v_fmac_f32_e32 v134, 0xba000000, v46
	v_fmac_f32_e32 v195, 0xba000000, v46
	v_fmac_f32_e32 v135, 0xba000000, v46
	v_fmac_f32_e32 v131, 0xba000000, v46
	v_fmac_f32_e32 v130, 0xba000000, v46
	v_fmac_f32_e32 v133, 0xba000000, v46
	v_fmac_f32_e32 v132, 0xba000000, v46
	v_fmac_f32_e32 v125, 0xba000000, v46
	v_fmac_f32_e32 v127, 0xba000000, v46
	v_fmac_f32_e32 v129, 0xba000000, v46
	v_fmac_f32_e32 v121, 0xba000000, v46
	v_fmac_f32_e32 v196, 0xba000000, v46
	v_fmac_f32_e32 v122, 0xba000000, v46
	v_fmac_f32_e32 v197, 0xba000000, v46
	v_fmac_f32_e32 v123, 0xba000000, v46
	v_fmac_f32_e32 v117, 0xba000000, v46
	v_fmac_f32_e32 v116, 0xba000000, v46
	v_fmac_f32_e32 v119, 0xba000000, v46
	v_fmac_f32_e32 v118, 0xba000000, v46
	v_fmac_f32_e32 v97, 0xba000000, v46
	v_fmac_f32_e32 v99, 0xba000000, v46
	v_fmac_f32_e32 v101, 0xba000000, v46
	v_fmac_f32_e32 v100, 0xba000000, v46
	s_nop 1
	v_pk_mul_f32 v[138:139], v[158:159], v[158:159]
	v_mov_b32_e32 v146, v157
	v_pk_fma_f32 v[144:145], v[156:157], v[156:157], v[138:139]
	v_mov_b32_e32 v157, v155
	s_waitcnt lgkmcnt(0)
; template <bool WB = true>
; __device__ __forceinline__ void ln1_phase(const bf16_t* buf, bf16_t* h1b, unsigned* xqs, float* sx, const float* gam, const float* bet, int G, int b) {
;     ...
;         for (int q = 0; q < R; ++q) { sq[q] = 0.f;
; #pragma unroll
;             for (int j = 0; j < 8; ++j) { v[q][j] = v[q][j] - sum[q]; sq[q] += (v[q][j].x * v[q][j].x + v[q][j].y * v[q][j].y) + (v[q][j].z * v[q][j].z + v[q][j].w * v[q][j].w); } }
; #pragma unroll
;         for (int q = 0; q < R; ++q) sq[q] = 1.0f / sqrtf(wave_sum(sq[q]) * (1.0f / D_) + LN_EPS);
	v_add_f32_dpp v10, v10, v10 quad_perm:[1,0,3,2] row_mask:0xf bank_mask:0xf
	s_nop 1
	v_mov_b32_e32 v139, v154
	v_pk_mul_f32 v[154:155], v[154:155], v[154:155]
	v_mov_b32_e32 v136, v156
	v_mov_b32_e32 v156, v153
	s_waitcnt lgkmcnt(0)
	v_add_f32_dpp v10, v10, v10 quad_perm:[2,3,0,1] row_mask:0xf bank_mask:0xf
	s_nop 1
	v_mov_b32_e32 v138, v152
	v_pk_fma_f32 v[152:153], v[152:153], v[152:153], v[154:155]
	v_mul_f32_e32 v40, v84, v84
	v_pk_add_f32 v[144:145], v[144:145], v[152:153]
	s_waitcnt lgkmcnt(0)
	v_add_f32_dpp v10, v10, v10 row_half_mirror row_mask:0xf bank_mask:0xf
	s_nop 1
	v_pk_mul_f32 v[152:153], v[186:187], v[186:187]
	v_pk_add_f32 v[144:145], v[144:145], v[144:145] op_sel_hi:[0,1]
	v_pk_mov_b32 v[154:155], v[150:151], v[152:153] op_sel:[1,0]
	v_mov_b32_e32 v151, v153
	s_waitcnt lgkmcnt(0)
	v_add_f32_dpp v10, v10, v10 row_mirror row_mask:0xf bank_mask:0xf
	s_nop 1
	v_pk_add_f32 v[150:151], v[154:155], v[150:151]
	v_pk_fma_f32 v[152:153], v[84:85], v[84:85], v[40:41] op_sel_hi:[1,1,0]
	v_mul_f32_e32 v40, v86, v86
	v_pk_add_f32 v[150:151], v[150:151], v[150:151] op_sel_hi:[0,1]
	s_waitcnt lgkmcnt(0)
	v_add_f32_dpp v10, v10, v10 row_bcast:15 row_mask:0xa bank_mask:0xf
	s_nop 1
	v_pk_fma_f32 v[154:155], v[86:87], v[86:87], v[40:41] op_sel_hi:[1,1,0]
	v_mul_f32_e32 v152, v69, v69
	v_mul_f32_e32 v154, v75, v75
	v_mul_f32_e32 v150, v73, v73
	s_waitcnt lgkmcnt(0)
	v_add_f32_dpp v10, v10, v10 row_bcast:31 row_mask:0xc bank_mask:0xf
	s_nop 1
	v_readlane_b32 s98, v10, 63
	s_nop 1
	v_mov_b32_e32 v10, s98
	v_fmamk_f32 v10, v10, 0x3a000000, v217
	v_cmp_gt_f32_e32 vcc, s45, v10
	v_mul_f32_e32 v46, 0x4f800000, v10
	v_mul_f32_e32 v144, v71, v71
	v_cndmask_b32_e32 v10, v10, v46, vcc
	v_sqrt_f32_e32 v46, v10
	v_pk_add_f32 v[152:153], v[152:153], v[154:155]
	v_pk_add_f32 v[144:145], v[150:151], v[144:145]
	v_mov_b32_e32 v150, v63
	v_add_u32_e32 v48, -1, v46
	v_fma_f32 v56, -v48, v46, v10
	v_cmp_ge_f32_e64 s[0:1], 0, v56
	v_add_u32_e32 v56, 1, v46
	v_mov_b32_e32 v151, v149
	v_cndmask_b32_e64 v48, v46, v48, s[0:1]
	v_fma_f32 v46, -v56, v46, v10
	v_cmp_lt_f32_e64 s[0:1], 0, v46
	v_mov_b32_e32 v63, v148
	v_pk_add_f32 v[144:145], v[152:153], v[144:145]
	v_cndmask_b32_e64 v46, v48, v56, s[0:1]
	v_mul_f32_e32 v48, 0x37800000, v46
	v_cndmask_b32_e32 v46, v46, v48, vcc
	v_cmp_class_f32_e32 vcc, v10, v218
	v_pk_mul_f32 v[152:153], v[150:151], v[150:151]
	v_pk_mul_f32 v[148:149], v[62:63], v[62:63]
	v_cndmask_b32_e32 v10, v46, v10, vcc
	v_div_scale_f32 v46, s[0:1], v10, v10, 1.0
	v_rcp_f32_e32 v48, v46
	v_pk_mov_b32 v[154:155], v[148:149], v[152:153] op_sel:[1,0]
	v_mov_b32_e32 v149, v153
	v_mul_f32_e32 v40, v52, v52
	v_fma_f32 v56, -v46, v48, 1.0
	v_pk_add_f32 v[148:149], v[154:155], v[148:149]
	v_pk_fma_f32 v[152:153], v[52:53], v[52:53], v[40:41] op_sel_hi:[1,1,0]
	v_mul_f32_e32 v40, v54, v54
	v_fmac_f32_e32 v48, v56, v48
	v_div_scale_f32 v56, vcc, 1.0, v10, 1.0
	v_pk_add_f32 v[144:145], v[144:145], v[144:145] op_sel_hi:[0,1]
	v_pk_add_f32 v[148:149], v[148:149], v[148:149] op_sel_hi:[0,1]
	v_pk_fma_f32 v[154:155], v[54:55], v[54:55], v[40:41] op_sel_hi:[1,1,0]
	v_mul_f32_e32 v58, v56, v48
	v_mul_f32_e32 v152, v50, v50
	v_mul_f32_e32 v154, v51, v51
	v_mul_f32_e32 v148, v49, v49
	v_mul_f32_e32 v144, v47, v47
	v_fma_f32 v60, -v46, v58, v56
	v_pk_add_f32 v[152:153], v[152:153], v[154:155]
	v_pk_add_f32 v[144:145], v[148:149], v[144:145]
	v_fmac_f32_e32 v58, v60, v48
	v_pk_add_f32 v[144:145], v[152:153], v[144:145]
	v_fma_f32 v46, -v46, v58, v56
	v_add_f32_e32 v42, v144, v145
	v_div_fmas_f32 v46, v46, v48, v58
	v_div_fixup_f32 v10, v46, v10, 1.0
	s_nop 1
	v_pk_mul_f32 v[152:153], v[170:171], v[170:171]
	v_pk_mul_f32 v[154:155], v[162:163], v[162:163]
	v_mov_b32_e32 v147, v159
	v_mov_b32_e32 v148, v165
	s_waitcnt lgkmcnt(0)
	v_add_f32_dpp v42, v42, v42 quad_perm:[1,0,3,2] row_mask:0xf bank_mask:0xf
	s_nop 1
	v_pk_fma_f32 v[152:153], v[164:165], v[164:165], v[152:153]
	v_mov_b32_e32 v159, v163
	v_mov_b32_e32 v165, v162
	v_pk_fma_f32 v[154:155], v[160:161], v[160:161], v[154:155]
	s_waitcnt lgkmcnt(0)
	v_add_f32_dpp v42, v42, v42 quad_perm:[2,3,0,1] row_mask:0xf bank_mask:0xf
	s_nop 1
	v_mov_b32_e32 v162, v105
	v_mov_b32_e32 v163, v173
	v_mov_b32_e32 v105, v172
	v_mov_b32_e32 v137, v158
	s_waitcnt lgkmcnt(0)
	v_add_f32_dpp v42, v42, v42 row_half_mirror row_mask:0xf bank_mask:0xf
	s_nop 1
	v_mov_b32_e32 v144, v164
	v_mov_b32_e32 v158, v161
	v_mov_b32_e32 v164, v160
	v_pk_add_f32 v[152:153], v[152:153], v[154:155]
	s_waitcnt lgkmcnt(0)
	v_add_f32_dpp v42, v42, v42 row_mirror row_mask:0xf bank_mask:0xf
	s_nop 1
	v_pk_mul_f32 v[154:155], v[162:163], v[162:163]
	v_pk_mul_f32 v[160:161], v[104:105], v[104:105]
	v_mov_b32_e32 v149, v171
	v_mov_b32_e32 v145, v170
	s_waitcnt lgkmcnt(0)
	v_add_f32_dpp v42, v42, v42 row_bcast:15 row_mask:0xa bank_mask:0xf
	s_nop 1
	v_pk_mov_b32 v[170:171], v[160:161], v[154:155] op_sel:[1,0]
	v_mov_b32_e32 v161, v155
	v_mul_f32_e32 v40, v112, v112
	v_pk_add_f32 v[154:155], v[170:171], v[160:161]
	s_waitcnt lgkmcnt(0)
; template <bool WB = true>
; __device__ __forceinline__ void ln1_phase(const bf16_t* buf, bf16_t* h1b, unsigned* xqs, float* sx, const float* gam, const float* bet, int G, int b) {
;     ...
;             for (int j = 0; j < 8; ++j) { v[q][j] = v[q][j] - sum[q]; sq[q] += (v[q][j].x * v[q][j].x + v[q][j].y * v[q][j].y) + (v[q][j].z * v[q][j].z + v[q][j].w * v[q][j].w); } }
; #pragma unroll
;         for (int q = 0; q < R; ++q) sq[q] = 1.0f / sqrtf(wave_sum(sq[q]) * (1.0f / D_) + LN_EPS);
; #pragma unroll
;         for (int j = 0; j < 8; ++j) {
;             const f32x4 gg = *(const f32x4*)(gam + 256 * j + 4 * lane), bb = *(const f32x4*)(bet + 256 * j + 4 * lane);
	v_add_f32_dpp v42, v42, v42 row_bcast:31 row_mask:0xc bank_mask:0xf
	s_nop 1
	v_readlane_b32 s98, v42, 63
	s_nop 1
	v_mov_b32_e32 v42, s98
	v_fmamk_f32 v42, v42, 0x3a000000, v217
	v_cmp_gt_f32_e32 vcc, s45, v42
	v_mul_f32_e32 v46, 0x4f800000, v42
	v_pk_fma_f32 v[160:161], v[112:113], v[112:113], v[40:41] op_sel_hi:[1,1,0]
	v_cndmask_b32_e32 v42, v42, v46, vcc
	v_sqrt_f32_e32 v46, v42
	v_mul_f32_e32 v40, v114, v114
	v_pk_add_f32 v[152:153], v[152:153], v[152:153] op_sel_hi:[0,1]
	v_pk_add_f32 v[154:155], v[154:155], v[154:155] op_sel_hi:[0,1]
	v_add_u32_e32 v48, -1, v46
	v_fma_f32 v56, -v48, v46, v42
	v_cmp_ge_f32_e64 s[0:1], 0, v56
	v_add_u32_e32 v56, 1, v46
	v_pk_fma_f32 v[170:171], v[114:115], v[114:115], v[40:41] op_sel_hi:[1,1,0]
	v_cndmask_b32_e64 v48, v46, v48, s[0:1]
	v_fma_f32 v46, -v56, v46, v42
	v_cmp_lt_f32_e64 s[0:1], 0, v46
	v_mul_f32_e32 v160, v91, v91
	v_mul_f32_e32 v170, v111, v111
	v_cndmask_b32_e64 v46, v48, v56, s[0:1]
	v_mul_f32_e32 v48, 0x37800000, v46
	v_cndmask_b32_e32 v46, v46, v48, vcc
	v_cmp_class_f32_e32 vcc, v42, v218
	v_mul_f32_e32 v154, v109, v109
	v_mul_f32_e32 v152, v107, v107
	v_cndmask_b32_e32 v42, v46, v42, vcc
	v_div_scale_f32 v46, s[0:1], v42, v42, 1.0
	v_rcp_f32_e32 v48, v46
	v_pk_add_f32 v[160:161], v[160:161], v[170:171]
	v_pk_add_f32 v[152:153], v[154:155], v[152:153]
	v_mul_f32_e32 v40, v92, v92
	v_pk_add_f32 v[152:153], v[160:161], v[152:153]
	v_mov_b32_e32 v160, v103
	v_mov_b32_e32 v161, v175
	v_mov_b32_e32 v103, v174
	v_pk_mul_f32 v[154:155], v[160:161], v[160:161]
	v_pk_mul_f32 v[170:171], v[102:103], v[102:103]
	v_fma_f32 v56, -v46, v48, 1.0
	v_pk_mov_b32 v[172:173], v[170:171], v[154:155] op_sel:[1,0]
	v_mov_b32_e32 v171, v155
	v_pk_add_f32 v[154:155], v[172:173], v[170:171]
	v_pk_fma_f32 v[170:171], v[92:93], v[92:93], v[40:41] op_sel_hi:[1,1,0]
	v_mul_f32_e32 v40, v94, v94
	v_fmac_f32_e32 v48, v56, v48
	v_div_scale_f32 v56, vcc, 1.0, v42, 1.0
	v_pk_add_f32 v[152:153], v[152:153], v[152:153] op_sel_hi:[0,1]
	v_pk_add_f32 v[154:155], v[154:155], v[154:155] op_sel_hi:[0,1]
	v_pk_fma_f32 v[172:173], v[94:95], v[94:95], v[40:41] op_sel_hi:[1,1,0]
	v_mul_f32_e32 v58, v56, v48
	v_mul_f32_e32 v170, v82, v82
	v_mul_f32_e32 v172, v83, v83
	v_mul_f32_e32 v154, v81, v81
	v_mul_f32_e32 v152, v79, v79
	v_fma_f32 v60, -v46, v58, v56
	v_pk_add_f32 v[170:171], v[170:171], v[172:173]
	v_pk_add_f32 v[152:153], v[154:155], v[152:153]
	v_fmac_f32_e32 v58, v60, v48
	v_pk_add_f32 v[152:153], v[170:171], v[152:153]
	v_fma_f32 v46, -v46, v58, v56
	v_add_f32_e32 v40, v152, v153
	v_div_fmas_f32 v46, v46, v48, v58
	v_div_fixup_f32 v42, v46, v42, 1.0
	s_nop 1
	v_pk_mul_f32 v[152:153], v[192:193], v[192:193]
	v_pk_mul_f32 v[154:155], v[188:189], v[188:189]
	v_mov_b32_e32 v199, v193
	v_mov_b32_e32 v170, v190
	s_waitcnt lgkmcnt(0)
	v_add_f32_dpp v40, v40, v40 quad_perm:[1,0,3,2] row_mask:0xf bank_mask:0xf
	s_nop 1
	v_mov_b32_e32 v171, v192
	v_pk_fma_f32 v[152:153], v[190:191], v[190:191], v[152:153]
	v_mov_b32_e32 v190, v179
	v_mov_b32_e32 v200, v178
	s_waitcnt lgkmcnt(0)
	v_add_f32_dpp v40, v40, v40 quad_perm:[2,3,0,1] row_mask:0xf bank_mask:0xf
	s_nop 1
	v_pk_fma_f32 v[154:155], v[178:179], v[178:179], v[154:155]
	v_mov_b32_e32 v192, v135
	v_mov_b32_e32 v193, v195
	v_mov_b32_e32 v135, v194
	s_waitcnt lgkmcnt(0)
	v_add_f32_dpp v40, v40, v40 row_half_mirror row_mask:0xf bank_mask:0xf
	s_nop 1
	v_mov_b32_e32 v178, v123
	v_mov_b32_e32 v179, v197
	v_mov_b32_e32 v123, v196
	s_waitcnt vmcnt(6)
	v_mov_b64_e32 v[194:195], v[224:225]
	v_mov_b64_e32 v[196:197], v[226:227]
	global_load_dwordx4 v[224:227], v[16:17], off offset:3072
	s_waitcnt vmcnt(6)
	v_mov_b64_e32 v[220:221], v[228:229]
	v_mov_b64_e32 v[222:223], v[230:231]
	global_load_dwordx4 v[228:231], v[20:21], off
	s_waitcnt lgkmcnt(0)
	v_add_f32_dpp v40, v40, v40 row_mirror row_mask:0xf bank_mask:0xf
	s_nop 1
	v_pk_add_f32 v[152:153], v[152:153], v[154:155]
	v_pk_mul_f32 v[154:155], v[192:193], v[192:193]
	v_pk_mul_f32 v[172:173], v[134:135], v[134:135]
	v_mul_f32_e32 v8, v130, v130
	s_waitcnt lgkmcnt(0)
	v_add_f32_dpp v40, v40, v40 row_bcast:15 row_mask:0xa bank_mask:0xf
	s_nop 1
	v_pk_mov_b32 v[174:175], v[172:173], v[154:155] op_sel:[1,0]
	v_mov_b32_e32 v173, v155
	v_pk_add_f32 v[154:155], v[174:175], v[172:173]
	v_pk_fma_f32 v[172:173], v[130:131], v[130:131], v[8:9] op_sel_hi:[1,1,0]
	s_waitcnt lgkmcnt(0)
; template <bool WB = true>
; __device__ __forceinline__ void ln1_phase(const bf16_t* buf, bf16_t* h1b, unsigned* xqs, float* sx, const float* gam, const float* bet, int G, int b) {
;     ...
;         for (int q = 0; q < R; ++q) sq[q] = 1.0f / sqrtf(wave_sum(sq[q]) * (1.0f / D_) + LN_EPS);
; #pragma unroll
;         for (int j = 0; j < 8; ++j) {
;             const f32x4 gg = *(const f32x4*)(gam + 256 * j + 4 * lane), bb = *(const f32x4*)(bet + 256 * j + 4 * lane);
; #pragma unroll
;             for (int q = 0; q < R; ++q) v[q][j] = v[q][j] * sq[q] * gg + bb;
	v_add_f32_dpp v40, v40, v40 row_bcast:31 row_mask:0xc bank_mask:0xf
	s_nop 1
	v_readlane_b32 s98, v40, 63
	s_nop 1
	v_mov_b32_e32 v40, s98
	v_fmamk_f32 v40, v40, 0x3a000000, v217
	v_cmp_gt_f32_e32 vcc, s45, v40
	v_mul_f32_e32 v46, 0x4f800000, v40
	v_mul_f32_e32 v8, v132, v132
	v_cndmask_b32_e32 v40, v40, v46, vcc
	v_sqrt_f32_e32 v46, v40
	v_pk_add_f32 v[152:153], v[152:153], v[152:153] op_sel_hi:[0,1]
	v_pk_add_f32 v[154:155], v[154:155], v[154:155] op_sel_hi:[0,1]
	v_pk_fma_f32 v[174:175], v[132:133], v[132:133], v[8:9] op_sel_hi:[1,1,0]
	v_add_u32_e32 v48, -1, v46
	v_fma_f32 v56, -v48, v46, v40
	v_cmp_ge_f32_e64 s[0:1], 0, v56
	v_add_u32_e32 v56, 1, v46
	v_mul_f32_e32 v172, v121, v121
	v_cndmask_b32_e64 v48, v46, v48, s[0:1]
	v_fma_f32 v46, -v56, v46, v40
	v_cmp_lt_f32_e64 s[0:1], 0, v46
	v_mul_f32_e32 v174, v129, v129
	v_mul_f32_e32 v154, v127, v127
	v_cndmask_b32_e64 v46, v48, v56, s[0:1]
	v_mul_f32_e32 v48, 0x37800000, v46
	v_cndmask_b32_e32 v46, v46, v48, vcc
	v_cmp_class_f32_e32 vcc, v40, v218
	v_mul_f32_e32 v152, v125, v125
	v_pk_add_f32 v[172:173], v[172:173], v[174:175]
	v_cndmask_b32_e32 v40, v46, v40, vcc
	v_div_scale_f32 v46, s[0:1], v40, v40, 1.0
	v_rcp_f32_e32 v48, v46
	v_pk_add_f32 v[152:153], v[154:155], v[152:153]
	v_pk_mul_f32 v[154:155], v[178:179], v[178:179]
	v_pk_add_f32 v[152:153], v[172:173], v[152:153]
	v_pk_mul_f32 v[172:173], v[122:123], v[122:123]
	v_mul_f32_e32 v8, v116, v116
	v_pk_mov_b32 v[174:175], v[172:173], v[154:155] op_sel:[1,0]
	v_mov_b32_e32 v173, v155
	v_fma_f32 v56, -v46, v48, 1.0
	v_pk_add_f32 v[154:155], v[174:175], v[172:173]
	v_pk_fma_f32 v[172:173], v[116:117], v[116:117], v[8:9] op_sel_hi:[1,1,0]
	v_mul_f32_e32 v8, v118, v118
	v_fmac_f32_e32 v48, v56, v48
	v_div_scale_f32 v56, vcc, 1.0, v40, 1.0
	v_pk_add_f32 v[152:153], v[152:153], v[152:153] op_sel_hi:[0,1]
	v_pk_add_f32 v[154:155], v[154:155], v[154:155] op_sel_hi:[0,1]
	v_pk_fma_f32 v[174:175], v[118:119], v[118:119], v[8:9] op_sel_hi:[1,1,0]
	v_mul_f32_e32 v58, v56, v48
	v_mul_f32_e32 v172, v100, v100
	v_mul_f32_e32 v174, v101, v101
	v_mul_f32_e32 v154, v99, v99
	v_mul_f32_e32 v152, v97, v97
	v_fma_f32 v60, -v46, v58, v56
	v_pk_add_f32 v[172:173], v[172:173], v[174:175]
	v_pk_add_f32 v[152:153], v[154:155], v[152:153]
	v_fmac_f32_e32 v58, v60, v48
	v_pk_add_f32 v[152:153], v[172:173], v[152:153]
	v_fma_f32 v46, -v46, v58, v56
	v_add_f32_e32 v8, v152, v153
	v_div_fmas_f32 v46, v46, v48, v58
	v_div_fixup_f32 v48, v46, v40, 1.0
	s_nop 1
	v_pk_mul_f32 v[152:153], v[184:185], v[10:11] op_sel_hi:[1,0]
	v_pk_mul_f32 v[136:137], v[136:137], v[42:43] op_sel_hi:[1,0]
	v_pk_mul_f32 v[138:139], v[138:139], v[42:43] op_sel_hi:[1,0]
	v_mov_b32_e32 v201, v188
	s_waitcnt lgkmcnt(0)
	v_add_f32_dpp v8, v8, v8 quad_perm:[1,0,3,2] row_mask:0xf bank_mask:0xf
	s_nop 1
	v_pk_mul_f32 v[142:143], v[142:143], v[10:11] op_sel_hi:[1,0]
	v_pk_fma_f32 v[174:175], v[152:153], v[194:195], v[220:221]
	v_pk_fma_f32 v[152:153], v[138:139], v[196:197], v[222:223]
	v_pk_fma_f32 v[154:155], v[136:137], v[194:195], v[220:221]
	s_waitcnt lgkmcnt(0)
	v_add_f32_dpp v8, v8, v8 quad_perm:[2,3,0,1] row_mask:0xf bank_mask:0xf
	s_nop 1
	v_pk_mul_f32 v[136:137], v[144:145], v[48:49] op_sel_hi:[1,0]
	v_pk_mul_f32 v[138:139], v[164:165], v[48:49] op_sel_hi:[1,0]
	v_pk_fma_f32 v[172:173], v[142:143], v[196:197], v[222:223]
	v_pk_fma_f32 v[142:143], v[196:197], v[138:139], v[222:223]
	s_waitcnt lgkmcnt(0)
	v_add_f32_dpp v8, v8, v8 row_half_mirror row_mask:0xf bank_mask:0xf
	s_nop 1
	v_pk_fma_f32 v[144:145], v[194:195], v[136:137], v[220:221]
	v_pk_mul_f32 v[146:147], v[146:147], v[42:43] op_sel_hi:[1,0]
	v_mov_b32_e32 v198, v191
	v_mov_b32_e32 v191, v189
	s_waitcnt lgkmcnt(0)
	v_add_f32_dpp v8, v8, v8 row_mirror row_mask:0xf bank_mask:0xf
	s_nop 1
	v_pk_mul_f32 v[164:165], v[180:181], v[10:11] op_sel_hi:[1,0]
	v_pk_mul_f32 v[156:157], v[156:157], v[42:43] op_sel_hi:[1,0]
	v_pk_mul_f32 v[76:77], v[76:77], v[10:11] op_sel_hi:[1,0]
	v_pk_mul_f32 v[176:177], v[176:177], v[10:11] op_sel_hi:[1,0]
	s_waitcnt lgkmcnt(0)
	v_add_f32_dpp v8, v8, v8 row_bcast:15 row_mask:0xa bank_mask:0xf
	s_nop 1
	v_pk_mul_f32 v[64:65], v[64:65], v[10:11] op_sel_hi:[1,0]
	v_pk_mul_f32 v[66:67], v[66:67], v[10:11] op_sel_hi:[1,0]
	v_mov_b32_e32 v128, v121
	v_mov_b32_e32 v124, v127
	s_waitcnt lgkmcnt(0)
	v_add_f32_dpp v8, v8, v8 row_bcast:31 row_mask:0xc bank_mask:0xf
	s_nop 1
	v_readlane_b32 s98, v8, 63
	s_nop 1
	v_mov_b32_e32 v8, s98
	v_fmamk_f32 v8, v8, 0x3a000000, v217
	v_cmp_gt_f32_e32 vcc, s45, v8
	v_mul_f32_e32 v40, 0x4f800000, v8
	v_pk_mul_f32 v[6:7], v[6:7], v[10:11] op_sel_hi:[1,0]
	v_cndmask_b32_e32 v8, v8, v40, vcc
	v_sqrt_f32_e32 v40, v8
	v_pk_mul_f32 v[2:3], v[2:3], v[10:11] op_sel_hi:[1,0]
	v_pk_mul_f32 v[4:5], v[4:5], v[10:11] op_sel_hi:[1,0]
	v_pk_mul_f32 v[44:45], v[44:45], v[10:11] op_sel_hi:[1,0]
	v_add_u32_e32 v46, -1, v40
	v_fma_f32 v56, -v46, v40, v8
	v_cmp_ge_f32_e64 s[0:1], 0, v56
	v_add_u32_e32 v56, 1, v40
	v_mov_b32_e32 v96, v99
	v_cndmask_b32_e64 v46, v40, v46, s[0:1]
	v_fma_f32 v40, -v56, v40, v8
	v_cmp_lt_f32_e64 s[0:1], 0, v40
	s_nop 1
	v_cndmask_b32_e64 v40, v46, v56, s[0:1]
	v_mul_f32_e32 v46, 0x37800000, v40
	v_cndmask_b32_e32 v40, v40, v46, vcc
	v_cmp_class_f32_e32 vcc, v8, v218
	s_nop 1
	v_cndmask_b32_e32 v8, v40, v8, vcc
	v_div_scale_f32 v40, s[0:1], v8, v8, 1.0
	v_rcp_f32_e32 v46, v40
	s_nop 0
	v_fma_f32 v56, -v40, v46, 1.0
	v_fmac_f32_e32 v46, v56, v46
	v_div_scale_f32 v56, vcc, 1.0, v8, 1.0
	v_mul_f32_e32 v58, v56, v46
	v_fma_f32 v60, -v40, v58, v56
	v_fmac_f32_e32 v58, v60, v46
	v_fma_f32 v40, -v40, v58, v56
	v_div_fmas_f32 v40, v40, v46, v58
	v_div_fixup_f32 v72, v40, v8, 1.0
	v_pk_mul_f32 v[138:139], v[170:171], v[72:73] op_sel_hi:[1,0]
	v_pk_mul_f32 v[136:137], v[200:201], v[72:73] op_sel_hi:[1,0]
	v_pk_fma_f32 v[138:139], v[194:195], v[138:139], v[220:221]
	v_pk_fma_f32 v[136:137], v[196:197], v[136:137], v[222:223]
	s_waitcnt vmcnt(6)
; template <bool WB = true>
; __device__ __forceinline__ void ln1_phase(const bf16_t* buf, bf16_t* h1b, unsigned* xqs, float* sx, const float* gam, const float* bet, int G, int b) {
;     ...
; #pragma unroll
;         for (int j = 0; j < 8; ++j) {
;             const f32x4 gg = *(const f32x4*)(gam + 256 * j + 4 * lane), bb = *(const f32x4*)(bet + 256 * j + 4 * lane);
; #pragma unroll
;             for (int q = 0; q < R; ++q) v[q][j] = v[q][j] * sq[q] * gg + bb;
;         }
; #pragma unroll
;         for (int q = 0; q < R; ++q) { amax[q] = 0.f;
; #pragma unroll
;             for (int j = 0; j < 8; ++j) amax[q] = fmaxf(amax[q], fmaxf(fmaxf(fabsf(v[q][j].x), fabsf(v[q][j].y)), fmaxf(fabsf(v[q][j].z), fabsf(v[q][j].w)))); }
	v_mov_b64_e32 v[194:195], v[232:233]
	v_mov_b64_e32 v[196:197], v[234:235]
	global_load_dwordx4 v[232:235], v[22:23], off
	s_waitcnt vmcnt(6)
	v_mov_b64_e32 v[220:221], v[236:237]
	v_mov_b64_e32 v[222:223], v[238:239]
	global_load_dwordx4 v[236:239], v[24:25], off
	v_pk_mul_f32 v[170:171], v[182:183], v[10:11] op_sel_hi:[1,0]
	v_mov_b32_e32 v60, v9
	v_mov_b32_e32 v56, v59
	v_pk_mul_f32 v[8:9], v[60:61], v[10:11] op_sel_hi:[1,0]
	v_pk_mul_f32 v[56:57], v[56:57], v[10:11] op_sel_hi:[1,0]
	v_mov_b32_e32 v40, v43
	v_pk_mul_f32 v[40:41], v[40:41], v[10:11] op_sel_hi:[1,0]
	v_mov_b32_e32 v46, v49
	v_pk_fma_f32 v[182:183], v[170:171], v[196:197], v[222:223]
	v_pk_fma_f32 v[170:171], v[146:147], v[194:195], v[220:221]
	v_pk_mul_f32 v[146:147], v[148:149], v[48:49] op_sel_hi:[1,0]
	v_pk_mul_f32 v[148:149], v[158:159], v[48:49] op_sel_hi:[1,0]
	v_pk_fma_f32 v[184:185], v[164:165], v[194:195], v[220:221]
	v_pk_fma_f32 v[164:165], v[156:157], v[196:197], v[222:223]
	v_pk_fma_f32 v[156:157], v[196:197], v[148:149], v[222:223]
	v_pk_fma_f32 v[158:159], v[194:195], v[146:147], v[220:221]
	v_pk_mul_f32 v[148:149], v[198:199], v[72:73] op_sel_hi:[1,0]
	v_pk_mul_f32 v[146:147], v[190:191], v[72:73] op_sel_hi:[1,0]
	v_pk_fma_f32 v[148:149], v[194:195], v[148:149], v[220:221]
	v_pk_fma_f32 v[146:147], v[196:197], v[146:147], v[222:223]
	s_waitcnt vmcnt(6)
	v_mov_b64_e32 v[194:195], v[244:245]
	v_mov_b64_e32 v[196:197], v[246:247]
	global_load_dwordx4 v[244:247], v[26:27], off
	s_waitcnt vmcnt(6)
	v_mov_b64_e32 v[198:199], v[248:249]
	v_mov_b64_e32 v[200:201], v[250:251]
	global_load_dwordx4 v[248:251], v[28:29], off
	v_pk_fma_f32 v[190:191], v[76:77], v[194:195], v[198:199]
	v_pk_mul_f32 v[76:77], v[88:89], v[42:43] op_sel_hi:[1,0]
	v_pk_mul_f32 v[88:89], v[186:187], v[42:43] op_sel_hi:[1,0]
	v_pk_fma_f32 v[188:189], v[176:177], v[196:197], v[200:201]
	v_pk_fma_f32 v[176:177], v[88:89], v[196:197], v[200:201]
	v_pk_fma_f32 v[180:181], v[76:77], v[194:195], v[198:199]
	v_pk_mul_f32 v[76:77], v[104:105], v[48:49] op_sel_hi:[1,0]
	v_pk_mul_f32 v[88:89], v[162:163], v[48:49] op_sel_hi:[1,0]
	v_pk_fma_f32 v[162:163], v[76:77], v[194:195], v[198:199]
	v_pk_fma_f32 v[104:105], v[88:89], v[196:197], v[200:201]
	v_pk_mul_f32 v[88:89], v[134:135], v[72:73] op_sel_hi:[1,0]
	v_pk_mul_f32 v[76:77], v[192:193], v[72:73] op_sel_hi:[1,0]
	v_pk_fma_f32 v[88:89], v[194:195], v[88:89], v[198:199]
	v_pk_fma_f32 v[76:77], v[196:197], v[76:77], v[200:201]
	s_waitcnt vmcnt(6)
	v_mov_b64_e32 v[196:197], v[252:253]
	v_mov_b64_e32 v[198:199], v[254:255]
	global_load_dwordx4 v[252:255], v[30:31], off
	s_waitcnt vmcnt(6)
	v_mov_b64_e32 v[220:221], v[224:225]
	v_mov_b64_e32 v[222:223], v[226:227]
	global_load_dwordx4 v[224:227], v[32:33], off
	v_pk_fma_f32 v[192:193], v[66:67], v[198:199], v[222:223]
	v_pk_fma_f32 v[194:195], v[64:65], v[196:197], v[220:221]
	v_pk_mul_f32 v[64:65], v[84:85], v[42:43] op_sel_hi:[1,0]
	v_pk_mul_f32 v[66:67], v[86:87], v[42:43] op_sel_hi:[1,0]
	v_pk_fma_f32 v[186:187], v[64:65], v[196:197], v[220:221]
	v_pk_fma_f32 v[134:135], v[66:67], v[198:199], v[222:223]
	v_pk_mul_f32 v[64:65], v[112:113], v[48:49] op_sel_hi:[1,0]
	v_pk_mul_f32 v[66:67], v[114:115], v[48:49] op_sel_hi:[1,0]
	v_pk_fma_f32 v[86:87], v[64:65], v[196:197], v[220:221]
	v_pk_fma_f32 v[84:85], v[66:67], v[198:199], v[222:223]
	v_pk_mul_f32 v[66:67], v[130:131], v[72:73] op_sel_hi:[1,0]
	v_pk_mul_f32 v[64:65], v[132:133], v[72:73] op_sel_hi:[1,0]
	v_pk_fma_f32 v[66:67], v[196:197], v[66:67], v[220:221]
	v_pk_fma_f32 v[64:65], v[198:199], v[64:65], v[222:223]
	s_waitcnt vmcnt(6)
	v_mov_b64_e32 v[196:197], v[228:229]
	v_mov_b64_e32 v[198:199], v[230:231]
	global_load_dwordx4 v[228:231], v[34:35], off
	s_waitcnt vmcnt(6)
	v_mov_b64_e32 v[220:221], v[232:233]
	v_mov_b64_e32 v[222:223], v[234:235]
	v_pk_fma_f32 v[114:115], v[56:57], v[198:199], v[222:223]
	v_pk_fma_f32 v[130:131], v[8:9], v[196:197], v[220:221]
	v_pk_mul_f32 v[8:9], v[74:75], v[42:43] op_sel_hi:[1,0]
	v_pk_mul_f32 v[56:57], v[70:71], v[42:43] op_sel_hi:[1,0]
	v_pk_fma_f32 v[112:113], v[8:9], v[196:197], v[220:221]
	v_pk_fma_f32 v[74:75], v[56:57], v[198:199], v[222:223]
	v_pk_mul_f32 v[8:9], v[110:111], v[48:49] op_sel_hi:[1,0]
	v_pk_mul_f32 v[56:57], v[106:107], v[48:49] op_sel_hi:[1,0]
	v_pk_fma_f32 v[68:69], v[8:9], v[196:197], v[220:221]
	v_pk_fma_f32 v[60:61], v[56:57], v[198:199], v[222:223]
	v_pk_mul_f32 v[8:9], v[128:129], v[72:73] op_sel_hi:[1,0]
	v_pk_mul_f32 v[56:57], v[124:125], v[72:73] op_sel_hi:[1,0]
	v_pk_fma_f32 v[58:59], v[196:197], v[8:9], v[220:221]
	v_pk_fma_f32 v[56:57], v[198:199], v[56:57], v[222:223]
	s_waitcnt vmcnt(5)
	v_mov_b64_e32 v[196:197], v[236:237]
	v_mov_b64_e32 v[198:199], v[238:239]
	s_waitcnt vmcnt(4)
	v_mov_b64_e32 v[220:221], v[244:245]
	v_mov_b64_e32 v[222:223], v[246:247]
	v_pk_mul_f32 v[8:9], v[140:141], v[10:11] op_sel_hi:[1,0]
	v_max_f32_e64 v10, |v84|, |v85|
	v_max3_f32 v10, |v86|, |v87|, v10
	v_pk_fma_f32 v[124:125], v[8:9], v[198:199], v[222:223]
	v_pk_fma_f32 v[126:127], v[6:7], v[196:197], v[220:221]
	v_pk_mul_f32 v[6:7], v[62:63], v[42:43] op_sel_hi:[1,0]
	v_pk_mul_f32 v[8:9], v[150:151], v[42:43] op_sel_hi:[1,0]
	v_pk_fma_f32 v[108:109], v[6:7], v[196:197], v[220:221]
	v_pk_fma_f32 v[106:107], v[8:9], v[198:199], v[222:223]
	v_pk_mul_f32 v[6:7], v[102:103], v[48:49] op_sel_hi:[1,0]
	v_pk_mul_f32 v[8:9], v[160:161], v[48:49] op_sel_hi:[1,0]
	v_pk_fma_f32 v[102:103], v[6:7], v[196:197], v[220:221]
	v_pk_fma_f32 v[90:91], v[8:9], v[198:199], v[222:223]
	v_pk_mul_f32 v[6:7], v[122:123], v[72:73] op_sel_hi:[1,0]
	v_pk_mul_f32 v[8:9], v[178:179], v[72:73] op_sel_hi:[1,0]
	v_pk_fma_f32 v[70:71], v[6:7], v[196:197], v[220:221]
	v_pk_fma_f32 v[62:63], v[8:9], v[198:199], v[222:223]
	s_waitcnt vmcnt(3)
; __device__ __forceinline__ unsigned pk2(float lo, float hi) { const f32x2c_t v = {lo, hi}; const bf16x2c_t b = __builtin_convertvector(v, bf16x2c_t); return __builtin_bit_cast(unsigned, b); }
; template <bool WB = true>
; __device__ __forceinline__ void ln1_phase(const bf16_t* buf, bf16_t* h1b, unsigned* xqs, float* sx, const float* gam, const float* bet, int G, int b) {
;     ...
; #pragma unroll
;         for (int q = 0; q < R; ++q) { amax[q] = 0.f;
; #pragma unroll
;             for (int j = 0; j < 8; ++j) amax[q] = fmaxf(amax[q], fmaxf(fmaxf(fabsf(v[q][j].x), fabsf(v[q][j].y)), fmaxf(fabsf(v[q][j].z), fabsf(v[q][j].w)))); }
; #pragma unroll
;         for (int q = 0; q < R; ++q) amax[q] = wave_max(amax[q]);
; #pragma unroll
;         for (int q = 0; q < R; ++q) {
;             const int row = row0 + q * NGW;
;             if (row < S_) {
;                 const float inv = amax[q] > 0.f ? 127.0f / amax[q] : 0.f;
;                 if (lane == 0) sx[row] = amax[q] * (1.0f / 127.0f);
; #pragma unroll
;                 for (int j = 0; j < 8; ++j) {
;                     if (WB) *(u32x2*)(h1b + (size_t)row * D_ + 256 * j + 4 * lane) = (u32x2){pk2(v[q][j].x, v[q][j].y), pk2(v[q][j].z, v[q][j].w)};
;                     xqs[((size_t)j * S_ + row) * 64 + lane] = pack_i8x4(v[q][j], inv);
	v_mov_b64_e32 v[6:7], v[248:249]
	v_mov_b64_e32 v[8:9], v[250:251]
	s_waitcnt vmcnt(2)
	v_mov_b64_e32 v[196:197], v[252:253]
	v_mov_b64_e32 v[198:199], v[254:255]
	v_pk_fma_f32 v[122:123], v[4:5], v[8:9], v[198:199]
	v_pk_fma_f32 v[128:129], v[2:3], v[6:7], v[196:197]
	v_pk_mul_f32 v[2:3], v[52:53], v[42:43] op_sel_hi:[1,0]
	v_pk_mul_f32 v[4:5], v[54:55], v[42:43] op_sel_hi:[1,0]
	v_pk_fma_f32 v[120:121], v[2:3], v[6:7], v[196:197]
	v_pk_fma_f32 v[110:111], v[4:5], v[8:9], v[198:199]
	v_pk_mul_f32 v[2:3], v[92:93], v[48:49] op_sel_hi:[1,0]
	v_pk_mul_f32 v[4:5], v[94:95], v[48:49] op_sel_hi:[1,0]
	v_pk_fma_f32 v[94:95], v[2:3], v[6:7], v[196:197]
	v_pk_fma_f32 v[92:93], v[4:5], v[8:9], v[198:199]
	v_pk_mul_f32 v[2:3], v[116:117], v[72:73] op_sel_hi:[1,0]
	v_pk_mul_f32 v[4:5], v[118:119], v[72:73] op_sel_hi:[1,0]
	v_pk_fma_f32 v[54:55], v[2:3], v[6:7], v[196:197]
	v_pk_fma_f32 v[52:53], v[4:5], v[8:9], v[198:199]
	s_waitcnt vmcnt(1)
	v_mov_b64_e32 v[2:3], v[224:225]
	v_mov_b64_e32 v[4:5], v[226:227]
	s_waitcnt vmcnt(0)
	v_mov_b64_e32 v[6:7], v[228:229]
	v_mov_b64_e32 v[8:9], v[230:231]
	v_pk_fma_f32 v[116:117], v[40:41], v[4:5], v[8:9]
	v_pk_mul_f32 v[40:41], v[50:51], v[42:43] op_sel_hi:[1,0]
	v_pk_mul_f32 v[42:43], v[46:47], v[42:43] op_sel_hi:[1,0]
	v_pk_fma_f32 v[118:119], v[44:45], v[2:3], v[6:7]
	v_pk_fma_f32 v[44:45], v[42:43], v[4:5], v[8:9]
	v_pk_fma_f32 v[46:47], v[40:41], v[2:3], v[6:7]
	v_pk_mul_f32 v[42:43], v[82:83], v[48:49] op_sel_hi:[1,0]
	v_pk_mul_f32 v[40:41], v[78:79], v[48:49] op_sel_hi:[1,0]
	v_pk_mul_f32 v[48:49], v[100:101], v[72:73] op_sel_hi:[1,0]
	v_pk_fma_f32 v[42:43], v[42:43], v[2:3], v[6:7]
	v_pk_fma_f32 v[2:3], v[48:49], v[2:3], v[6:7]
	v_max_f32_e64 v6, |v172|, |v173|
	v_max_f32_e64 v7, |v182|, |v183|
	v_pk_mul_f32 v[50:51], v[96:97], v[72:73] op_sel_hi:[1,0]
	v_max3_f32 v6, |v174|, |v175|, v6
	v_max3_f32 v7, |v184|, |v185|, v7
	v_pk_fma_f32 v[40:41], v[40:41], v[4:5], v[8:9]
	v_pk_fma_f32 v[4:5], v[50:51], v[4:5], v[8:9]
	v_max3_f32 v6, v6, 0, v7
	v_max_f32_e64 v7, |v188|, |v189|
	v_max_f32_e64 v8, |v192|, |v193|
	v_max3_f32 v7, |v190|, |v191|, v7
	v_max3_f32 v8, |v194|, |v195|, v8
	v_max3_f32 v6, v6, v7, v8
	v_max_f32_e64 v7, |v114|, |v115|
	v_max_f32_e64 v8, |v124|, |v125|
	v_max3_f32 v7, |v130|, |v131|, v7
	v_max3_f32 v8, |v126|, |v127|, v8
	v_max3_f32 v6, v6, v7, v8
	v_max_f32_e64 v7, |v122|, |v123|
	v_max_f32_e64 v8, |v116|, |v117|
	v_max3_f32 v7, |v128|, |v129|, v7
	v_max3_f32 v8, |v118|, |v119|, v8
	v_max3_f32 v6, v6, v7, v8
	v_max_f32_e64 v7, |v152|, |v153|
	v_max_f32_e64 v8, |v164|, |v165|
	v_max3_f32 v7, |v154|, |v155|, v7
	v_max3_f32 v8, |v170|, |v171|, v8
	v_max3_f32 v7, v7, 0, v8
	v_max_f32_e64 v8, |v176|, |v177|
	v_max_f32_e64 v9, |v134|, |v135|
	v_max3_f32 v8, |v180|, |v181|, v8
	v_max3_f32 v9, |v186|, |v187|, v9
	v_max3_f32 v7, v7, v8, v9
	v_max_f32_e64 v8, |v74|, |v75|
	v_max_f32_e64 v9, |v106|, |v107|
	v_max3_f32 v8, |v112|, |v113|, v8
	v_max3_f32 v9, |v108|, |v109|, v9
	v_max3_f32 v7, v7, v8, v9
	v_max_f32_e64 v8, |v110|, |v111|
	v_max_f32_e64 v9, |v44|, |v45|
	v_max3_f32 v8, |v120|, |v121|, v8
	v_max3_f32 v9, |v46|, |v47|, v9
	v_max3_f32 v7, v7, v8, v9
	v_max_f32_e64 v8, |v142|, |v143|
	v_max_f32_e64 v9, |v156|, |v157|
	v_max3_f32 v8, |v144|, |v145|, v8
	v_max3_f32 v9, |v158|, |v159|, v9
	v_max3_f32 v8, v8, 0, v9
	v_max_f32_e64 v9, |v104|, |v105|
	v_max3_f32 v9, |v162|, |v163|, v9
	v_max3_f32 v8, v8, v9, v10
	v_max_f32_e64 v9, |v60|, |v61|
	v_max_f32_e64 v10, |v90|, |v91|
	v_max3_f32 v9, |v68|, |v69|, v9
	v_max3_f32 v10, |v102|, |v103|, v10
	v_max3_f32 v8, v8, v9, v10
	v_max_f32_e64 v9, |v92|, |v93|
	v_max_f32_e64 v10, |v40|, |v41|
	v_max3_f32 v9, |v94|, |v95|, v9
	v_max3_f32 v10, |v42|, |v43|, v10
	v_max3_f32 v8, v8, v9, v10
	v_max_f32_e64 v9, |v136|, |v137|
	v_max_f32_e64 v10, |v146|, |v147|
	v_max3_f32 v9, |v138|, |v139|, v9
	v_max3_f32 v10, |v148|, |v149|, v10
	v_max3_f32 v9, v9, 0, v10
	v_max_f32_e64 v10, |v76|, |v77|
	v_max_f32_e64 v48, |v64|, |v65|
	v_max3_f32 v10, |v88|, |v89|, v10
	v_max3_f32 v48, |v66|, |v67|, v48
	v_max3_f32 v9, v9, v10, v48
	v_max_f32_e64 v10, |v56|, |v57|
	v_max_f32_e64 v48, |v62|, |v63|
	v_max3_f32 v10, |v58|, |v59|, v10
	v_max3_f32 v48, |v70|, |v71|, v48
	v_max3_f32 v9, v9, v10, v48
	v_max_f32_e64 v10, |v52|, |v53|
	v_max_f32_e64 v48, |v4|, |v5|
	v_max3_f32 v10, |v54|, |v55|, v10
	v_max3_f32 v48, |v2|, |v3|, v48
	v_max3_f32 v9, v9, v10, v48
	s_nop 1
	v_max_f32_dpp v6, v6, v6 quad_perm:[1,0,3,2] row_mask:0xf bank_mask:0xf
	v_max_f32_dpp v7, v7, v7 quad_perm:[1,0,3,2] row_mask:0xf bank_mask:0xf
	v_max_f32_dpp v8, v8, v8 quad_perm:[1,0,3,2] row_mask:0xf bank_mask:0xf
	v_max_f32_dpp v9, v9, v9 quad_perm:[1,0,3,2] row_mask:0xf bank_mask:0xf
	v_max_f32_dpp v6, v6, v6 quad_perm:[2,3,0,1] row_mask:0xf bank_mask:0xf
	v_max_f32_dpp v7, v7, v7 quad_perm:[2,3,0,1] row_mask:0xf bank_mask:0xf
	v_max_f32_dpp v8, v8, v8 quad_perm:[2,3,0,1] row_mask:0xf bank_mask:0xf
	v_max_f32_dpp v9, v9, v9 quad_perm:[2,3,0,1] row_mask:0xf bank_mask:0xf
	v_max_f32_dpp v6, v6, v6 row_half_mirror row_mask:0xf bank_mask:0xf
	v_max_f32_dpp v7, v7, v7 row_half_mirror row_mask:0xf bank_mask:0xf
	v_max_f32_dpp v8, v8, v8 row_half_mirror row_mask:0xf bank_mask:0xf
	v_max_f32_dpp v9, v9, v9 row_half_mirror row_mask:0xf bank_mask:0xf
	v_max_f32_dpp v6, v6, v6 row_mirror row_mask:0xf bank_mask:0xf
	v_max_f32_dpp v7, v7, v7 row_mirror row_mask:0xf bank_mask:0xf
	v_max_f32_dpp v8, v8, v8 row_mirror row_mask:0xf bank_mask:0xf
	v_max_f32_dpp v9, v9, v9 row_mirror row_mask:0xf bank_mask:0xf
	v_max_f32_dpp v6, v6, v6 row_bcast:15 row_mask:0xa bank_mask:0xf
	v_max_f32_dpp v7, v7, v7 row_bcast:15 row_mask:0xa bank_mask:0xf
	v_max_f32_dpp v8, v8, v8 row_bcast:15 row_mask:0xa bank_mask:0xf
	v_max_f32_dpp v9, v9, v9 row_bcast:15 row_mask:0xa bank_mask:0xf
	v_max_f32_dpp v6, v6, v6 row_bcast:31 row_mask:0xc bank_mask:0xf
	v_max_f32_dpp v7, v7, v7 row_bcast:31 row_mask:0xc bank_mask:0xf
	v_max_f32_dpp v8, v8, v8 row_bcast:31 row_mask:0xc bank_mask:0xf
	v_max_f32_dpp v9, v9, v9 row_bcast:31 row_mask:0xc bank_mask:0xf
	s_nop 1
	v_readlane_b32 s98, v6, 63
	v_readlane_b32 s99, v7, 63
	v_readlane_b32 s0, v8, 63
	v_readlane_b32 s1, v9, 63
	s_nop 1
	v_mov_b32_e32 v10, s98
	v_mov_b32_e32 v48, s99
	v_mov_b32_e32 v49, s99
	v_mov_b32_e32 v6, s0
	v_mov_b32_e32 v7, s0
	v_mov_b32_e32 v8, s1
	v_mov_b32_e32 v9, s1
	s_waitcnt lgkmcnt(0)
	s_and_saveexec_b64 s[0:1], s[38:39]
	s_cbranch_execz .LBB0_545
	s_add_u32 s8, s92, s6
	v_mul_f32_e32 v50, 0x3c010204, v10
	s_addc_u32 s9, s93, s7
	global_store_dword v11, v50, s[8:9]
